# baseline (speedup 1.0000x reference)
.LBB1_30:
	s_and_b64 vcc, exec, s[4:5]
	s_cbranch_vccz .LBB1_41
	s_load_dwordx4 s[44:47], s[0:1], 0x0
	s_load_dwordx2 s[48:49], s[0:1], 0x20
	s_add_i32 s50, s2, 0xffffff40
	v_and_b32_e32 v1, 63, v0
	v_lshrrev_b32_e32 v2, 6, v0
	v_lshlrev_b32_e32 v3, 4, v1
	v_lshl_add_u32 v3, v2, 13, v3
	v_add_u32_e32 v3, 0x1000, v3
	v_lshlrev_b32_e32 v4, 3, v1
	v_lshl_add_u32 v4, v2, 12, v4
	v_add_u32_e32 v4, 0x800, v4
	s_waitcnt lgkmcnt(0)
	s_add_u32 s48, s48, 0x408000
	s_addc_u32 s49, s49, 0
	s_load_dwordx4 s[52:55], s[48:49], 0x400
	s_lshl_b32 s51, s50, 18
	s_add_u32 s44, s44, s51
	s_addc_u32 s45, s45, 0
	s_mul_i32 s51, s50, 0x30000
	s_add_u32 s46, s46, s51
	s_addc_u32 s47, s47, 0
	s_waitcnt lgkmcnt(0)
	s_lshl_b32 s51, s50, 19
	s_add_u32 s52, s52, s51
	s_addc_u32 s53, s53, 0
	s_mul_i32 s51, s50, 0x60000
	s_add_u32 s54, s54, s51
	s_addc_u32 s55, s55, 0
	v_cmp_eq_u32_e64 s[78:79], 0, v0
	v_mov_b32_e32 v5, 1
	v_mov_b32_e32 v6, s50
	v_lshlrev_b32_e32 v6, 2, v6
	s_add_u32 s58, s52, 0x0
	s_addc_u32 s59, s53, 0
	global_load_dwordx4 v[16:19], v3, s[58:59] nt
	s_add_u32 s58, s52, 0x10000
	s_addc_u32 s59, s53, 0
	global_load_dwordx4 v[20:23], v3, s[58:59] nt
	s_add_u32 s58, s52, 0x20000
	s_addc_u32 s59, s53, 0
	global_load_dwordx4 v[24:27], v3, s[58:59] nt
	s_add_u32 s58, s52, 0x30000
	s_addc_u32 s59, s53, 0
	global_load_dwordx4 v[28:31], v3, s[58:59] nt
	s_add_u32 s58, s52, 0x40000
	s_addc_u32 s59, s53, 0
	global_load_dwordx4 v[32:35], v3, s[58:59] nt
	s_add_u32 s58, s52, 0x50000
	s_addc_u32 s59, s53, 0
	global_load_dwordx4 v[36:39], v3, s[58:59] nt
	s_add_u32 s58, s52, 0x60000
	s_addc_u32 s59, s53, 0
	global_load_dwordx4 v[40:43], v3, s[58:59] nt
	s_add_u32 s58, s52, 0x70000
	s_addc_u32 s59, s53, 0
	global_load_dwordx4 v[44:47], v3, s[58:59] nt
	s_add_u32 s58, s54, 0x0
	s_addc_u32 s59, s55, 0
	global_load_dwordx4 v[48:51], v3, s[58:59] nt
	s_add_u32 s58, s54, 0x10000
	s_addc_u32 s59, s55, 0
	global_load_dwordx4 v[52:55], v3, s[58:59] nt
	s_add_u32 s58, s54, 0x20000
	s_addc_u32 s59, s55, 0
	global_load_dwordx4 v[56:59], v3, s[58:59] nt
	s_add_u32 s58, s54, 0x30000
	s_addc_u32 s59, s55, 0
	global_load_dwordx4 v[60:63], v3, s[58:59] nt
	s_add_u32 s58, s54, 0x40000
	s_addc_u32 s59, s55, 0
	global_load_dwordx4 v[64:67], v3, s[58:59] nt
	s_add_u32 s58, s54, 0x50000
	s_addc_u32 s59, s55, 0
	global_load_dwordx4 v[68:71], v3, s[58:59] nt
	s_add_u32 s58, s52, 0x400
	s_addc_u32 s59, s53, 0
	global_load_dwordx4 v[72:75], v3, s[58:59] nt
	s_add_u32 s58, s52, 0x10400
	s_addc_u32 s59, s53, 0
	global_load_dwordx4 v[76:79], v3, s[58:59] nt
	s_add_u32 s58, s52, 0x20400
	s_addc_u32 s59, s53, 0
	global_load_dwordx4 v[80:83], v3, s[58:59] nt
	s_add_u32 s58, s52, 0x30400
	s_addc_u32 s59, s53, 0
	global_load_dwordx4 v[84:87], v3, s[58:59] nt
	s_add_u32 s58, s52, 0x40400
	s_addc_u32 s59, s53, 0
	global_load_dwordx4 v[88:91], v3, s[58:59] nt
	s_add_u32 s58, s52, 0x50400
	s_addc_u32 s59, s53, 0
	global_load_dwordx4 v[92:95], v3, s[58:59] nt
	s_add_u32 s58, s52, 0x60400
	s_addc_u32 s59, s53, 0
	global_load_dwordx4 v[96:99], v3, s[58:59] nt
	s_add_u32 s58, s52, 0x70400
	s_addc_u32 s59, s53, 0
	global_load_dwordx4 v[100:103], v3, s[58:59] nt
	s_add_u32 s58, s54, 0x400
	s_addc_u32 s59, s55, 0
	global_load_dwordx4 v[104:107], v3, s[58:59] nt
	s_add_u32 s58, s54, 0x10400
	s_addc_u32 s59, s55, 0
	global_load_dwordx4 v[108:111], v3, s[58:59] nt
	s_add_u32 s58, s54, 0x20400
	s_addc_u32 s59, s55, 0
	global_load_dwordx4 v[112:115], v3, s[58:59] nt
	s_add_u32 s58, s54, 0x30400
	s_addc_u32 s59, s55, 0
	global_load_dwordx4 v[116:119], v3, s[58:59] nt
	s_add_u32 s58, s54, 0x40400
	s_addc_u32 s59, s55, 0
	global_load_dwordx4 v[120:123], v3, s[58:59] nt
	s_add_u32 s58, s54, 0x50400
	s_addc_u32 s59, s55, 0
	global_load_dwordx4 v[124:127], v3, s[58:59] nt
	s_waitcnt vmcnt(27)
	v_cvt_pk_f16_f32 v16, v16, v17
	v_cvt_pk_f16_f32 v17, v18, v19
	s_add_u32 s76, s44, 0x0
	s_addc_u32 s77, s45, 0
	global_store_dwordx2 v4, v[16:17], s[76:77] sc1
	s_waitcnt vmcnt(27)
	v_cvt_pk_f16_f32 v20, v20, v21
	v_cvt_pk_f16_f32 v21, v22, v23
	s_add_u32 s76, s44, 0x8000
	s_addc_u32 s77, s45, 0
	global_store_dwordx2 v4, v[20:21], s[76:77] sc1
	s_waitcnt vmcnt(27)
	v_cvt_pk_f16_f32 v24, v24, v25
	v_cvt_pk_f16_f32 v25, v26, v27
	s_add_u32 s76, s44, 0x10000
	s_addc_u32 s77, s45, 0
	global_store_dwordx2 v4, v[24:25], s[76:77] sc1
	s_waitcnt vmcnt(27)
	v_cvt_pk_f16_f32 v28, v28, v29
	v_cvt_pk_f16_f32 v29, v30, v31
	s_add_u32 s76, s44, 0x18000
	s_addc_u32 s77, s45, 0
	global_store_dwordx2 v4, v[28:29], s[76:77] sc1
	s_waitcnt vmcnt(27)
	v_cvt_pk_f16_f32 v32, v32, v33
	v_cvt_pk_f16_f32 v33, v34, v35
	s_add_u32 s76, s44, 0x20000
	s_addc_u32 s77, s45, 0
	global_store_dwordx2 v4, v[32:33], s[76:77] sc1
	s_waitcnt vmcnt(27)
	v_cvt_pk_f16_f32 v36, v36, v37
	v_cvt_pk_f16_f32 v37, v38, v39
	s_add_u32 s76, s44, 0x28000
	s_addc_u32 s77, s45, 0
	global_store_dwordx2 v4, v[36:37], s[76:77] sc1
	s_waitcnt vmcnt(27)
	v_cvt_pk_f16_f32 v40, v40, v41
	v_cvt_pk_f16_f32 v41, v42, v43
	s_add_u32 s76, s44, 0x30000
	s_addc_u32 s77, s45, 0
	global_store_dwordx2 v4, v[40:41], s[76:77] sc1
	s_waitcnt vmcnt(27)
	v_cvt_pk_f16_f32 v44, v44, v45
	v_cvt_pk_f16_f32 v45, v46, v47
	s_add_u32 s76, s44, 0x38000
	s_addc_u32 s77, s45, 0
	global_store_dwordx2 v4, v[44:45], s[76:77] sc1
	s_waitcnt vmcnt(27)
	v_cvt_pk_f16_f32 v48, v48, v49
	v_cvt_pk_f16_f32 v49, v50, v51
	s_add_u32 s76, s46, 0x0
	s_addc_u32 s77, s47, 0
	global_store_dwordx2 v4, v[48:49], s[76:77] sc1
	s_waitcnt vmcnt(27)
	v_cvt_pk_f16_f32 v52, v52, v53
	v_cvt_pk_f16_f32 v53, v54, v55
	s_add_u32 s76, s46, 0x8000
	s_addc_u32 s77, s47, 0
	global_store_dwordx2 v4, v[52:53], s[76:77] sc1
	s_waitcnt vmcnt(27)
	v_cvt_pk_f16_f32 v56, v56, v57
	v_cvt_pk_f16_f32 v57, v58, v59
	s_add_u32 s76, s46, 0x10000
	s_addc_u32 s77, s47, 0
	global_store_dwordx2 v4, v[56:57], s[76:77] sc1
	s_waitcnt vmcnt(27)
	v_cvt_pk_f16_f32 v60, v60, v61
	v_cvt_pk_f16_f32 v61, v62, v63
	s_add_u32 s76, s46, 0x18000
	s_addc_u32 s77, s47, 0
	global_store_dwordx2 v4, v[60:61], s[76:77] sc1
	s_waitcnt vmcnt(27)
	v_cvt_pk_f16_f32 v64, v64, v65
	v_cvt_pk_f16_f32 v65, v66, v67
	s_add_u32 s76, s46, 0x20000
	s_addc_u32 s77, s47, 0
	global_store_dwordx2 v4, v[64:65], s[76:77] sc1
	s_waitcnt vmcnt(27)
	v_cvt_pk_f16_f32 v68, v68, v69
	v_cvt_pk_f16_f32 v69, v70, v71
	s_add_u32 s76, s46, 0x28000
	s_addc_u32 s77, s47, 0
	global_store_dwordx2 v4, v[68:69], s[76:77] sc1
	s_add_u32 s58, s52, 0x800
	s_addc_u32 s59, s53, 0
	global_load_dwordx4 v[16:19], v3, s[58:59] nt
	s_add_u32 s58, s52, 0x10800
	s_addc_u32 s59, s53, 0
	global_load_dwordx4 v[20:23], v3, s[58:59] nt
	s_add_u32 s58, s52, 0x20800
	s_addc_u32 s59, s53, 0
	global_load_dwordx4 v[24:27], v3, s[58:59] nt
	s_add_u32 s58, s52, 0x30800
	s_addc_u32 s59, s53, 0
	global_load_dwordx4 v[28:31], v3, s[58:59] nt
	s_add_u32 s58, s52, 0x40800
	s_addc_u32 s59, s53, 0
	global_load_dwordx4 v[32:35], v3, s[58:59] nt
	s_add_u32 s58, s52, 0x50800
	s_addc_u32 s59, s53, 0
	global_load_dwordx4 v[36:39], v3, s[58:59] nt
	s_add_u32 s58, s52, 0x60800
	s_addc_u32 s59, s53, 0
	global_load_dwordx4 v[40:43], v3, s[58:59] nt
	s_add_u32 s58, s52, 0x70800
	s_addc_u32 s59, s53, 0
	global_load_dwordx4 v[44:47], v3, s[58:59] nt
	s_add_u32 s58, s54, 0x800
	s_addc_u32 s59, s55, 0
	global_load_dwordx4 v[48:51], v3, s[58:59] nt
	s_add_u32 s58, s54, 0x10800
	s_addc_u32 s59, s55, 0
	global_load_dwordx4 v[52:55], v3, s[58:59] nt
	s_add_u32 s58, s54, 0x20800
	s_addc_u32 s59, s55, 0
	global_load_dwordx4 v[56:59], v3, s[58:59] nt
	s_add_u32 s58, s54, 0x30800
	s_addc_u32 s59, s55, 0
	global_load_dwordx4 v[60:63], v3, s[58:59] nt
	s_add_u32 s58, s54, 0x40800
	s_addc_u32 s59, s55, 0
	global_load_dwordx4 v[64:67], v3, s[58:59] nt
	s_add_u32 s58, s54, 0x50800
	s_addc_u32 s59, s55, 0
	global_load_dwordx4 v[68:71], v3, s[58:59] nt
	s_waitcnt vmcnt(41)
	v_cvt_pk_f16_f32 v72, v72, v73
	v_cvt_pk_f16_f32 v73, v74, v75
	s_add_u32 s76, s44, 0x200
	s_addc_u32 s77, s45, 0
	global_store_dwordx2 v4, v[72:73], s[76:77] sc1
	s_waitcnt vmcnt(41)
	v_cvt_pk_f16_f32 v76, v76, v77
	v_cvt_pk_f16_f32 v77, v78, v79
	s_add_u32 s76, s44, 0x8200
	s_addc_u32 s77, s45, 0
	global_store_dwordx2 v4, v[76:77], s[76:77] sc1
	s_waitcnt vmcnt(41)
	v_cvt_pk_f16_f32 v80, v80, v81
	v_cvt_pk_f16_f32 v81, v82, v83
	s_add_u32 s76, s44, 0x10200
	s_addc_u32 s77, s45, 0
	global_store_dwordx2 v4, v[80:81], s[76:77] sc1
	s_waitcnt vmcnt(41)
	v_cvt_pk_f16_f32 v84, v84, v85
	v_cvt_pk_f16_f32 v85, v86, v87
	s_add_u32 s76, s44, 0x18200
	s_addc_u32 s77, s45, 0
	global_store_dwordx2 v4, v[84:85], s[76:77] sc1
	s_waitcnt vmcnt(41)
	v_cvt_pk_f16_f32 v88, v88, v89
	v_cvt_pk_f16_f32 v89, v90, v91
	s_add_u32 s76, s44, 0x20200
	s_addc_u32 s77, s45, 0
	global_store_dwordx2 v4, v[88:89], s[76:77] sc1
	s_waitcnt vmcnt(41)
	v_cvt_pk_f16_f32 v92, v92, v93
	v_cvt_pk_f16_f32 v93, v94, v95
	s_add_u32 s76, s44, 0x28200
	s_addc_u32 s77, s45, 0
	global_store_dwordx2 v4, v[92:93], s[76:77] sc1
	s_waitcnt vmcnt(41)
	v_cvt_pk_f16_f32 v96, v96, v97
	v_cvt_pk_f16_f32 v97, v98, v99
	s_add_u32 s76, s44, 0x30200
	s_addc_u32 s77, s45, 0
	global_store_dwordx2 v4, v[96:97], s[76:77] sc1
	s_waitcnt vmcnt(41)
	v_cvt_pk_f16_f32 v100, v100, v101
	v_cvt_pk_f16_f32 v101, v102, v103
	s_add_u32 s76, s44, 0x38200
	s_addc_u32 s77, s45, 0
	global_store_dwordx2 v4, v[100:101], s[76:77] sc1
	s_waitcnt vmcnt(41)
	v_cvt_pk_f16_f32 v104, v104, v105
	v_cvt_pk_f16_f32 v105, v106, v107
	s_add_u32 s76, s46, 0x200
	s_addc_u32 s77, s47, 0
	global_store_dwordx2 v4, v[104:105], s[76:77] sc1
	s_waitcnt vmcnt(41)
	v_cvt_pk_f16_f32 v108, v108, v109
	v_cvt_pk_f16_f32 v109, v110, v111
	s_add_u32 s76, s46, 0x8200
	s_addc_u32 s77, s47, 0
	global_store_dwordx2 v4, v[108:109], s[76:77] sc1
	s_waitcnt vmcnt(41)
	v_cvt_pk_f16_f32 v112, v112, v113
	v_cvt_pk_f16_f32 v113, v114, v115
	s_add_u32 s76, s46, 0x10200
	s_addc_u32 s77, s47, 0
	global_store_dwordx2 v4, v[112:113], s[76:77] sc1
	s_waitcnt vmcnt(41)
	v_cvt_pk_f16_f32 v116, v116, v117
	v_cvt_pk_f16_f32 v117, v118, v119
	s_add_u32 s76, s46, 0x18200
	s_addc_u32 s77, s47, 0
	global_store_dwordx2 v4, v[116:117], s[76:77] sc1
	s_waitcnt vmcnt(41)
	v_cvt_pk_f16_f32 v120, v120, v121
	v_cvt_pk_f16_f32 v121, v122, v123
	s_add_u32 s76, s46, 0x20200
	s_addc_u32 s77, s47, 0
	global_store_dwordx2 v4, v[120:121], s[76:77] sc1
	s_waitcnt vmcnt(41)
	v_cvt_pk_f16_f32 v124, v124, v125
	v_cvt_pk_f16_f32 v125, v126, v127
	s_add_u32 s76, s46, 0x28200
	s_addc_u32 s77, s47, 0
	global_store_dwordx2 v4, v[124:125], s[76:77] sc1
	s_waitcnt vmcnt(28)
	s_barrier
	s_mov_b64 s[56:57], exec
	s_and_b64 exec, exec, s[78:79]
	global_store_dword v6, v5, s[48:49] offset:0 sc1
	s_mov_b64 exec, s[56:57]
	s_add_u32 s58, s52, 0xc00
	s_addc_u32 s59, s53, 0
	global_load_dwordx4 v[72:75], v3, s[58:59] nt
	s_add_u32 s58, s52, 0x10c00
	s_addc_u32 s59, s53, 0
	global_load_dwordx4 v[76:79], v3, s[58:59] nt
	s_add_u32 s58, s52, 0x20c00
	s_addc_u32 s59, s53, 0
	global_load_dwordx4 v[80:83], v3, s[58:59] nt
	s_add_u32 s58, s52, 0x30c00
	s_addc_u32 s59, s53, 0
	global_load_dwordx4 v[84:87], v3, s[58:59] nt
	s_add_u32 s58, s52, 0x40c00
	s_addc_u32 s59, s53, 0
	global_load_dwordx4 v[88:91], v3, s[58:59] nt
	s_add_u32 s58, s52, 0x50c00
	s_addc_u32 s59, s53, 0
	global_load_dwordx4 v[92:95], v3, s[58:59] nt
	s_add_u32 s58, s52, 0x60c00
	s_addc_u32 s59, s53, 0
	global_load_dwordx4 v[96:99], v3, s[58:59] nt
	s_add_u32 s58, s52, 0x70c00
	s_addc_u32 s59, s53, 0
	global_load_dwordx4 v[100:103], v3, s[58:59] nt
	s_add_u32 s58, s54, 0xc00
	s_addc_u32 s59, s55, 0
	global_load_dwordx4 v[104:107], v3, s[58:59] nt
	s_add_u32 s58, s54, 0x10c00
	s_addc_u32 s59, s55, 0
	global_load_dwordx4 v[108:111], v3, s[58:59] nt
	s_add_u32 s58, s54, 0x20c00
	s_addc_u32 s59, s55, 0
	global_load_dwordx4 v[112:115], v3, s[58:59] nt
	s_add_u32 s58, s54, 0x30c00
	s_addc_u32 s59, s55, 0
	global_load_dwordx4 v[116:119], v3, s[58:59] nt
	s_add_u32 s58, s54, 0x40c00
	s_addc_u32 s59, s55, 0
	global_load_dwordx4 v[120:123], v3, s[58:59] nt
	s_add_u32 s58, s54, 0x50c00
	s_addc_u32 s59, s55, 0
	global_load_dwordx4 v[124:127], v3, s[58:59] nt
	s_waitcnt vmcnt(42)
	v_cvt_pk_f16_f32 v16, v16, v17
	v_cvt_pk_f16_f32 v17, v18, v19
	s_add_u32 s76, s44, 0x400
	s_addc_u32 s77, s45, 0
	global_store_dwordx2 v4, v[16:17], s[76:77] sc1
	s_waitcnt vmcnt(42)
	v_cvt_pk_f16_f32 v20, v20, v21
	v_cvt_pk_f16_f32 v21, v22, v23
	s_add_u32 s76, s44, 0x8400
	s_addc_u32 s77, s45, 0
	global_store_dwordx2 v4, v[20:21], s[76:77] sc1
	s_waitcnt vmcnt(42)
	v_cvt_pk_f16_f32 v24, v24, v25
	v_cvt_pk_f16_f32 v25, v26, v27
	s_add_u32 s76, s44, 0x10400
	s_addc_u32 s77, s45, 0
	global_store_dwordx2 v4, v[24:25], s[76:77] sc1
	s_waitcnt vmcnt(42)
	v_cvt_pk_f16_f32 v28, v28, v29
	v_cvt_pk_f16_f32 v29, v30, v31
	s_add_u32 s76, s44, 0x18400
	s_addc_u32 s77, s45, 0
	global_store_dwordx2 v4, v[28:29], s[76:77] sc1
	s_waitcnt vmcnt(42)
	v_cvt_pk_f16_f32 v32, v32, v33
	v_cvt_pk_f16_f32 v33, v34, v35
	s_add_u32 s76, s44, 0x20400
	s_addc_u32 s77, s45, 0
	global_store_dwordx2 v4, v[32:33], s[76:77] sc1
	s_waitcnt vmcnt(42)
	v_cvt_pk_f16_f32 v36, v36, v37
	v_cvt_pk_f16_f32 v37, v38, v39
	s_add_u32 s76, s44, 0x28400
	s_addc_u32 s77, s45, 0
	global_store_dwordx2 v4, v[36:37], s[76:77] sc1
	s_waitcnt vmcnt(42)
	v_cvt_pk_f16_f32 v40, v40, v41
	v_cvt_pk_f16_f32 v41, v42, v43
	s_add_u32 s76, s44, 0x30400
	s_addc_u32 s77, s45, 0
	global_store_dwordx2 v4, v[40:41], s[76:77] sc1
	s_waitcnt vmcnt(42)
	v_cvt_pk_f16_f32 v44, v44, v45
	v_cvt_pk_f16_f32 v45, v46, v47
	s_add_u32 s76, s44, 0x38400
	s_addc_u32 s77, s45, 0
	global_store_dwordx2 v4, v[44:45], s[76:77] sc1
	s_waitcnt vmcnt(42)
	v_cvt_pk_f16_f32 v48, v48, v49
	v_cvt_pk_f16_f32 v49, v50, v51
	s_add_u32 s76, s46, 0x400
	s_addc_u32 s77, s47, 0
	global_store_dwordx2 v4, v[48:49], s[76:77] sc1
	s_waitcnt vmcnt(42)
	v_cvt_pk_f16_f32 v52, v52, v53
	v_cvt_pk_f16_f32 v53, v54, v55
	s_add_u32 s76, s46, 0x8400
	s_addc_u32 s77, s47, 0
	global_store_dwordx2 v4, v[52:53], s[76:77] sc1
	s_waitcnt vmcnt(42)
	v_cvt_pk_f16_f32 v56, v56, v57
	v_cvt_pk_f16_f32 v57, v58, v59
	s_add_u32 s76, s46, 0x10400
	s_addc_u32 s77, s47, 0
	global_store_dwordx2 v4, v[56:57], s[76:77] sc1
	s_waitcnt vmcnt(42)
	v_cvt_pk_f16_f32 v60, v60, v61
	v_cvt_pk_f16_f32 v61, v62, v63
	s_add_u32 s76, s46, 0x18400
	s_addc_u32 s77, s47, 0
	global_store_dwordx2 v4, v[60:61], s[76:77] sc1
	s_waitcnt vmcnt(42)
	v_cvt_pk_f16_f32 v64, v64, v65
	v_cvt_pk_f16_f32 v65, v66, v67
	s_add_u32 s76, s46, 0x20400
	s_addc_u32 s77, s47, 0
	global_store_dwordx2 v4, v[64:65], s[76:77] sc1
	s_waitcnt vmcnt(42)
	v_cvt_pk_f16_f32 v68, v68, v69
	v_cvt_pk_f16_f32 v69, v70, v71
	s_add_u32 s76, s46, 0x28400
	s_addc_u32 s77, s47, 0
	global_store_dwordx2 v4, v[68:69], s[76:77] sc1
	s_waitcnt vmcnt(29)
	s_barrier
	s_mov_b64 s[56:57], exec
	s_and_b64 exec, exec, s[78:79]
	global_store_dword v6, v5, s[48:49] offset:256 sc1
	s_mov_b64 exec, s[56:57]
	s_waitcnt vmcnt(28)
	v_cvt_pk_f16_f32 v72, v72, v73
	v_cvt_pk_f16_f32 v73, v74, v75
	s_add_u32 s76, s44, 0x600
	s_addc_u32 s77, s45, 0
	global_store_dwordx2 v4, v[72:73], s[76:77] sc1
	s_waitcnt vmcnt(28)
	v_cvt_pk_f16_f32 v76, v76, v77
	v_cvt_pk_f16_f32 v77, v78, v79
	s_add_u32 s76, s44, 0x8600
	s_addc_u32 s77, s45, 0
	global_store_dwordx2 v4, v[76:77], s[76:77] sc1
	s_waitcnt vmcnt(28)
	v_cvt_pk_f16_f32 v80, v80, v81
	v_cvt_pk_f16_f32 v81, v82, v83
	s_add_u32 s76, s44, 0x10600
	s_addc_u32 s77, s45, 0
	global_store_dwordx2 v4, v[80:81], s[76:77] sc1
	s_waitcnt vmcnt(28)
	v_cvt_pk_f16_f32 v84, v84, v85
	v_cvt_pk_f16_f32 v85, v86, v87
	s_add_u32 s76, s44, 0x18600
	s_addc_u32 s77, s45, 0
	global_store_dwordx2 v4, v[84:85], s[76:77] sc1
	s_waitcnt vmcnt(28)
	v_cvt_pk_f16_f32 v88, v88, v89
	v_cvt_pk_f16_f32 v89, v90, v91
	s_add_u32 s76, s44, 0x20600
	s_addc_u32 s77, s45, 0
	global_store_dwordx2 v4, v[88:89], s[76:77] sc1
	s_waitcnt vmcnt(28)
	v_cvt_pk_f16_f32 v92, v92, v93
	v_cvt_pk_f16_f32 v93, v94, v95
	s_add_u32 s76, s44, 0x28600
	s_addc_u32 s77, s45, 0
	global_store_dwordx2 v4, v[92:93], s[76:77] sc1
	s_waitcnt vmcnt(28)
	v_cvt_pk_f16_f32 v96, v96, v97
	v_cvt_pk_f16_f32 v97, v98, v99
	s_add_u32 s76, s44, 0x30600
	s_addc_u32 s77, s45, 0
	global_store_dwordx2 v4, v[96:97], s[76:77] sc1
	s_waitcnt vmcnt(28)
	v_cvt_pk_f16_f32 v100, v100, v101
	v_cvt_pk_f16_f32 v101, v102, v103
	s_add_u32 s76, s44, 0x38600
	s_addc_u32 s77, s45, 0
	global_store_dwordx2 v4, v[100:101], s[76:77] sc1
	s_waitcnt vmcnt(28)
	v_cvt_pk_f16_f32 v104, v104, v105
	v_cvt_pk_f16_f32 v105, v106, v107
	s_add_u32 s76, s46, 0x600
	s_addc_u32 s77, s47, 0
	global_store_dwordx2 v4, v[104:105], s[76:77] sc1
	s_waitcnt vmcnt(28)
	v_cvt_pk_f16_f32 v108, v108, v109
	v_cvt_pk_f16_f32 v109, v110, v111
	s_add_u32 s76, s46, 0x8600
	s_addc_u32 s77, s47, 0
	global_store_dwordx2 v4, v[108:109], s[76:77] sc1
	s_waitcnt vmcnt(28)
	v_cvt_pk_f16_f32 v112, v112, v113
	v_cvt_pk_f16_f32 v113, v114, v115
	s_add_u32 s76, s46, 0x10600
	s_addc_u32 s77, s47, 0
	global_store_dwordx2 v4, v[112:113], s[76:77] sc1
	s_waitcnt vmcnt(28)
	v_cvt_pk_f16_f32 v116, v116, v117
	v_cvt_pk_f16_f32 v117, v118, v119
	s_add_u32 s76, s46, 0x18600
	s_addc_u32 s77, s47, 0
	global_store_dwordx2 v4, v[116:117], s[76:77] sc1
	s_waitcnt vmcnt(28)
	v_cvt_pk_f16_f32 v120, v120, v121
	v_cvt_pk_f16_f32 v121, v122, v123
	s_add_u32 s76, s46, 0x20600
	s_addc_u32 s77, s47, 0
	global_store_dwordx2 v4, v[120:121], s[76:77] sc1
	s_waitcnt vmcnt(28)
	v_cvt_pk_f16_f32 v124, v124, v125
	v_cvt_pk_f16_f32 v125, v126, v127
	s_add_u32 s76, s46, 0x28600
	s_addc_u32 s77, s47, 0
	global_store_dwordx2 v4, v[124:125], s[76:77] sc1
	s_waitcnt vmcnt(15)
	s_barrier
	s_mov_b64 s[56:57], exec
	s_and_b64 exec, exec, s[78:79]
	global_store_dword v6, v5, s[48:49] offset:512 sc1
	s_mov_b64 exec, s[56:57]
	s_waitcnt vmcnt(1)
	s_barrier
	s_mov_b64 s[56:57], exec
	s_and_b64 exec, exec, s[78:79]
	global_store_dword v6, v5, s[48:49] offset:768 sc1
	s_mov_b64 exec, s[56:57]
	s_add_i32 s24, s2, 0xffffff40
	s_lshl_b32 s20, s24, 4
	s_lshl_b32 s0, s24, 5
	s_ashr_i32 s21, s20, 31
	s_and_b32 s25, s0, 0xffffffc0
	s_lshl_b64 s[20:21], s[20:21], 2
	v_lshrrev_b32_e32 v6, 6, v0
	s_waitcnt lgkmcnt(0)
	s_add_u32 s26, s30, s20
	s_addc_u32 s27, s31, s21
	v_lshl_or_b32 v2, v6, 3, s25
	s_and_b32 s25, s2, 1
	s_lshl_b32 s2, s25, 7
	s_add_u32 s20, s28, s2
	v_and_b32_e32 v7, 63, v0
	s_mov_b32 s3, 0
	s_addc_u32 s21, s29, 0
	s_bfe_u32 s2, s24, 0x1a0001
	v_add_u32_e32 v2, v2, v7
	v_mov_b32_e32 v3, 0
	s_lshl_b64 s[2:3], s[2:3], 19
	v_lshl_add_u32 v1, v6, 2, 0
	v_lshlrev_b64 v[4:5], 8, v[2:3]
	v_lshl_or_b32 v2, v6, 16, s2
	s_lshl_b32 s2, s25, 12
	v_lshlrev_b32_e32 v6, 2, v7
	v_cmp_gt_u32_e64 s[0:1], 8, v7
	v_cmp_eq_u32_e64 s[22:23], 0, v7
	v_cmp_eq_u32_e64 s[6:7], 1, v7
	v_cmp_eq_u32_e64 s[8:9], 2, v7
	v_cmp_eq_u32_e64 s[10:11], 3, v7
	v_cmp_eq_u32_e64 s[12:13], 4, v7
	v_cmp_eq_u32_e64 s[14:15], 5, v7
	v_cmp_eq_u32_e64 s[16:17], 6, v7
	v_cmp_eq_u32_e64 s[18:19], 7, v7
	v_or3_b32 v6, v2, s2, v6
	v_mov_b32_e32 v7, s3
	v_cmp_eq_u32_e64 s[4:5], 0, v0
	v_lshl_add_u64 v[4:5], s[20:21], 0, v[4:5]
	v_lshl_add_u64 v[6:7], s[42:43], 0, v[6:7]
	s_mov_b64 s[28:29], 0
	s_lshr_b32 s58, s24, 1
	s_lshl_b32 s58, s58, 19
	s_add_u32 s60, s42, s58
	s_addc_u32 s61, s43, 0
	s_add_u32 s62, s60, 0x2000
	s_addc_u32 s63, s61, 0
	s_add_u32 s64, s62, 0x2000
	s_addc_u32 s65, s63, 0
	s_add_u32 s66, s64, 0x2000
	s_addc_u32 s67, s65, 0
	s_add_u32 s68, s66, 0x2000
	s_addc_u32 s69, s67, 0
	s_add_u32 s70, s68, 0x2000
	s_addc_u32 s71, s69, 0
	s_add_u32 s72, s70, 0x2000
	s_addc_u32 s73, s71, 0
	s_add_u32 s74, s72, 0x2000
	s_addc_u32 s75, s73, 0
	v_lshrrev_b32_e32 v96, 6, v0
	v_lshlrev_b32_e32 v96, 16, v96
	v_and_b32_e32 v97, 63, v0
	v_lshl_add_u32 v96, v97, 2, v96
	s_and_b32 s59, s24, 1
	s_lshl_b32 s59, s59, 12
	v_add_u32_e32 v96, s59, v96
	s_mov_b32 s76, 0
	s_mov_b32 s77, 0
	global_load_dword v100, v96, s[60:61] offset:0 nt
	global_load_dword v101, v96, s[62:63] offset:0 nt
	global_load_dword v102, v96, s[64:65] offset:0 nt
	global_load_dword v103, v96, s[66:67] offset:0 nt
	global_load_dword v104, v96, s[68:69] offset:0 nt
	global_load_dword v105, v96, s[70:71] offset:0 nt
	global_load_dword v106, v96, s[72:73] offset:0 nt
	global_load_dword v107, v96, s[74:75] offset:0 nt
	global_load_dword v108, v96, s[60:61] offset:256 nt
	global_load_dword v109, v96, s[62:63] offset:256 nt
	global_load_dword v110, v96, s[64:65] offset:256 nt
	global_load_dword v111, v96, s[66:67] offset:256 nt
	global_load_dword v112, v96, s[68:69] offset:256 nt
	global_load_dword v113, v96, s[70:71] offset:256 nt
	global_load_dword v114, v96, s[72:73] offset:256 nt
	global_load_dword v115, v96, s[74:75] offset:256 nt
	global_load_dword v116, v96, s[60:61] offset:512 nt
	global_load_dword v117, v96, s[62:63] offset:512 nt
	global_load_dword v118, v96, s[64:65] offset:512 nt
	global_load_dword v119, v96, s[66:67] offset:512 nt
	global_load_dword v120, v96, s[68:69] offset:512 nt
	global_load_dword v121, v96, s[70:71] offset:512 nt
	global_load_dword v122, v96, s[72:73] offset:512 nt
	global_load_dword v123, v96, s[74:75] offset:512 nt
	global_load_dword v124, v96, s[60:61] offset:768 nt
	global_load_dword v125, v96, s[62:63] offset:768 nt
	global_load_dword v126, v96, s[64:65] offset:768 nt
	global_load_dword v127, v96, s[66:67] offset:768 nt
	global_load_dword v128, v96, s[68:69] offset:768 nt
	global_load_dword v129, v96, s[70:71] offset:768 nt
	global_load_dword v130, v96, s[72:73] offset:768 nt
	global_load_dword v131, v96, s[74:75] offset:768 nt
	global_load_dword v132, v96, s[60:61] offset:1024 nt
	global_load_dword v133, v96, s[62:63] offset:1024 nt
	global_load_dword v134, v96, s[64:65] offset:1024 nt
	global_load_dword v135, v96, s[66:67] offset:1024 nt
	global_load_dword v136, v96, s[68:69] offset:1024 nt
	global_load_dword v137, v96, s[70:71] offset:1024 nt
	global_load_dword v138, v96, s[72:73] offset:1024 nt
	global_load_dword v139, v96, s[74:75] offset:1024 nt
	global_load_dword v140, v96, s[60:61] offset:1280 nt
	global_load_dword v141, v96, s[62:63] offset:1280 nt
	global_load_dword v142, v96, s[64:65] offset:1280 nt
	global_load_dword v143, v96, s[66:67] offset:1280 nt
	global_load_dword v144, v96, s[68:69] offset:1280 nt
	global_load_dword v145, v96, s[70:71] offset:1280 nt
	global_load_dword v146, v96, s[72:73] offset:1280 nt
	global_load_dword v147, v96, s[74:75] offset:1280 nt
	global_load_dword v148, v96, s[60:61] offset:1536 nt
	global_load_dword v149, v96, s[62:63] offset:1536 nt
	global_load_dword v150, v96, s[64:65] offset:1536 nt
	global_load_dword v151, v96, s[66:67] offset:1536 nt
	global_load_dword v152, v96, s[68:69] offset:1536 nt
	global_load_dword v153, v96, s[70:71] offset:1536 nt
	global_load_dword v154, v96, s[72:73] offset:1536 nt
	global_load_dword v155, v96, s[74:75] offset:1536 nt
	s_waitcnt vmcnt(48)
	v_cmp_ne_u32_e32 vcc, 0, v100
	s_nop 1
	v_mov_b32_e32 v2, vcc_lo
	v_mov_b32_e32 v9, vcc_hi
	v_cmp_ne_u32_e32 vcc, 0, v101
	v_cndmask_b32_e64 v2, 0, v2, s[22:23]
	v_cndmask_b32_e64 v9, 0, v9, s[22:23]
	v_mov_b32_e32 v11, vcc_hi
	v_mov_b32_e32 v14, vcc_lo
	v_cndmask_b32_e64 v9, v9, v11, s[6:7]
	v_cndmask_b32_e64 v2, v2, v14, s[6:7]
	v_cmp_ne_u32_e32 vcc, 0, v102
	s_nop 1
	v_mov_b32_e32 v11, vcc_lo
	v_mov_b32_e32 v14, vcc_hi
	v_cmp_ne_u32_e32 vcc, 0, v103
	v_cndmask_b32_e64 v2, v2, v11, s[8:9]
	v_cndmask_b32_e64 v9, v9, v14, s[8:9]
	v_mov_b32_e32 v11, vcc_hi
	v_mov_b32_e32 v14, vcc_lo
	v_cmp_ne_u32_e32 vcc, 0, v104
	v_cndmask_b32_e64 v9, v9, v11, s[10:11]
	v_cndmask_b32_e64 v2, v2, v14, s[10:11]
	v_mov_b32_e32 v11, vcc_lo
	v_mov_b32_e32 v12, vcc_hi
	v_cmp_ne_u32_e32 vcc, 0, v105
	v_cndmask_b32_e64 v2, v2, v11, s[12:13]
	v_cndmask_b32_e64 v9, v9, v12, s[12:13]
	v_mov_b32_e32 v11, vcc_hi
	v_mov_b32_e32 v12, vcc_lo
	v_cndmask_b32_e64 v9, v9, v11, s[14:15]
	v_cndmask_b32_e64 v2, v2, v12, s[14:15]
	v_cmp_ne_u32_e32 vcc, 0, v106
	s_nop 1
	v_mov_b32_e32 v10, vcc_lo
	v_mov_b32_e32 v11, vcc_hi
	v_cmp_ne_u32_e32 vcc, 0, v107
	v_cndmask_b32_e64 v2, v2, v10, s[16:17]
	v_cndmask_b32_e64 v8, v9, v11, s[16:17]
	v_mov_b32_e32 v9, vcc_hi
	v_mov_b32_e32 v10, vcc_lo
	v_cndmask_b32_e64 v9, v8, v9, s[18:19]
	v_cndmask_b32_e64 v8, v2, v10, s[18:19]
	s_mov_b64 s[2:3], exec
	s_mov_b64 exec, s[0:1]
	global_store_dwordx2 v[4:5], v[8:9], off
	s_mov_b64 exec, s[2:3]
	v_cmp_ne_u64_e32 vcc, 0, v[8:9]
	s_and_b64 s[20:21], s[0:1], vcc
	s_cmp_lg_u64 s[20:21], 0
	s_cselect_b32 s20, 1, 0
	s_or_b32 s76, s76, s20
	v_cmp_ne_u64_e32 vcc, -1, v[8:9]
	s_and_b64 s[20:21], s[0:1], vcc
	s_cmp_lg_u64 s[20:21], 0
	s_cselect_b32 s20, 1, 0
	s_or_b32 s77, s77, s20
	v_lshl_add_u64 v[4:5], v[4:5], 0, 8
	global_load_dword v156, v96, s[60:61] offset:1792 nt
	global_load_dword v157, v96, s[62:63] offset:1792 nt
	global_load_dword v158, v96, s[64:65] offset:1792 nt
	global_load_dword v159, v96, s[66:67] offset:1792 nt
	global_load_dword v160, v96, s[68:69] offset:1792 nt
	global_load_dword v161, v96, s[70:71] offset:1792 nt
	global_load_dword v162, v96, s[72:73] offset:1792 nt
	global_load_dword v163, v96, s[74:75] offset:1792 nt
	s_waitcnt vmcnt(49)
	v_cmp_ne_u32_e32 vcc, 0, v108
	s_nop 1
	v_mov_b32_e32 v2, vcc_lo
	v_mov_b32_e32 v9, vcc_hi
	v_cmp_ne_u32_e32 vcc, 0, v109
	v_cndmask_b32_e64 v2, 0, v2, s[22:23]
	v_cndmask_b32_e64 v9, 0, v9, s[22:23]
	v_mov_b32_e32 v11, vcc_hi
	v_mov_b32_e32 v14, vcc_lo
	v_cndmask_b32_e64 v9, v9, v11, s[6:7]
	v_cndmask_b32_e64 v2, v2, v14, s[6:7]
	v_cmp_ne_u32_e32 vcc, 0, v110
	s_nop 1
	v_mov_b32_e32 v11, vcc_lo
	v_mov_b32_e32 v14, vcc_hi
	v_cmp_ne_u32_e32 vcc, 0, v111
	v_cndmask_b32_e64 v2, v2, v11, s[8:9]
	v_cndmask_b32_e64 v9, v9, v14, s[8:9]
	v_mov_b32_e32 v11, vcc_hi
	v_mov_b32_e32 v14, vcc_lo
	v_cmp_ne_u32_e32 vcc, 0, v112
	v_cndmask_b32_e64 v9, v9, v11, s[10:11]
	v_cndmask_b32_e64 v2, v2, v14, s[10:11]
	v_mov_b32_e32 v11, vcc_lo
	v_mov_b32_e32 v12, vcc_hi
	v_cmp_ne_u32_e32 vcc, 0, v113
	v_cndmask_b32_e64 v2, v2, v11, s[12:13]
	v_cndmask_b32_e64 v9, v9, v12, s[12:13]
	v_mov_b32_e32 v11, vcc_hi
	v_mov_b32_e32 v12, vcc_lo
	v_cndmask_b32_e64 v9, v9, v11, s[14:15]
	v_cndmask_b32_e64 v2, v2, v12, s[14:15]
	v_cmp_ne_u32_e32 vcc, 0, v114
	s_nop 1
	v_mov_b32_e32 v10, vcc_lo
	v_mov_b32_e32 v11, vcc_hi
	v_cmp_ne_u32_e32 vcc, 0, v115
	v_cndmask_b32_e64 v2, v2, v10, s[16:17]
	v_cndmask_b32_e64 v8, v9, v11, s[16:17]
	v_mov_b32_e32 v9, vcc_hi
	v_mov_b32_e32 v10, vcc_lo
	v_cndmask_b32_e64 v9, v8, v9, s[18:19]
	v_cndmask_b32_e64 v8, v2, v10, s[18:19]
	s_mov_b64 s[2:3], exec
	s_mov_b64 exec, s[0:1]
	global_store_dwordx2 v[4:5], v[8:9], off
	s_mov_b64 exec, s[2:3]
	v_cmp_ne_u64_e32 vcc, 0, v[8:9]
	s_and_b64 s[20:21], s[0:1], vcc
	s_cmp_lg_u64 s[20:21], 0
	s_cselect_b32 s20, 2, 0
	s_or_b32 s76, s76, s20
	v_cmp_ne_u64_e32 vcc, -1, v[8:9]
	s_and_b64 s[20:21], s[0:1], vcc
	s_cmp_lg_u64 s[20:21], 0
	s_cselect_b32 s20, 2, 0
	s_or_b32 s77, s77, s20
	v_lshl_add_u64 v[4:5], v[4:5], 0, 8
	global_load_dword v164, v96, s[60:61] offset:2048 nt
	global_load_dword v165, v96, s[62:63] offset:2048 nt
	global_load_dword v166, v96, s[64:65] offset:2048 nt
	global_load_dword v167, v96, s[66:67] offset:2048 nt
	global_load_dword v168, v96, s[68:69] offset:2048 nt
	global_load_dword v169, v96, s[70:71] offset:2048 nt
	global_load_dword v170, v96, s[72:73] offset:2048 nt
	global_load_dword v171, v96, s[74:75] offset:2048 nt
	s_waitcnt vmcnt(50)
	v_cmp_ne_u32_e32 vcc, 0, v116
	s_nop 1
	v_mov_b32_e32 v2, vcc_lo
	v_mov_b32_e32 v9, vcc_hi
	v_cmp_ne_u32_e32 vcc, 0, v117
	v_cndmask_b32_e64 v2, 0, v2, s[22:23]
	v_cndmask_b32_e64 v9, 0, v9, s[22:23]
	v_mov_b32_e32 v11, vcc_hi
	v_mov_b32_e32 v14, vcc_lo
	v_cndmask_b32_e64 v9, v9, v11, s[6:7]
	v_cndmask_b32_e64 v2, v2, v14, s[6:7]
	v_cmp_ne_u32_e32 vcc, 0, v118
	s_nop 1
	v_mov_b32_e32 v11, vcc_lo
	v_mov_b32_e32 v14, vcc_hi
	v_cmp_ne_u32_e32 vcc, 0, v119
	v_cndmask_b32_e64 v2, v2, v11, s[8:9]
	v_cndmask_b32_e64 v9, v9, v14, s[8:9]
	v_mov_b32_e32 v11, vcc_hi
	v_mov_b32_e32 v14, vcc_lo
	v_cmp_ne_u32_e32 vcc, 0, v120
	v_cndmask_b32_e64 v9, v9, v11, s[10:11]
	v_cndmask_b32_e64 v2, v2, v14, s[10:11]
	v_mov_b32_e32 v11, vcc_lo
	v_mov_b32_e32 v12, vcc_hi
	v_cmp_ne_u32_e32 vcc, 0, v121
	v_cndmask_b32_e64 v2, v2, v11, s[12:13]
	v_cndmask_b32_e64 v9, v9, v12, s[12:13]
	v_mov_b32_e32 v11, vcc_hi
	v_mov_b32_e32 v12, vcc_lo
	v_cndmask_b32_e64 v9, v9, v11, s[14:15]
	v_cndmask_b32_e64 v2, v2, v12, s[14:15]
	v_cmp_ne_u32_e32 vcc, 0, v122
	s_nop 1
	v_mov_b32_e32 v10, vcc_lo
	v_mov_b32_e32 v11, vcc_hi
	v_cmp_ne_u32_e32 vcc, 0, v123
	v_cndmask_b32_e64 v2, v2, v10, s[16:17]
	v_cndmask_b32_e64 v8, v9, v11, s[16:17]
	v_mov_b32_e32 v9, vcc_hi
	v_mov_b32_e32 v10, vcc_lo
	v_cndmask_b32_e64 v9, v8, v9, s[18:19]
	v_cndmask_b32_e64 v8, v2, v10, s[18:19]
	s_mov_b64 s[2:3], exec
	s_mov_b64 exec, s[0:1]
	global_store_dwordx2 v[4:5], v[8:9], off
	s_mov_b64 exec, s[2:3]
	v_cmp_ne_u64_e32 vcc, 0, v[8:9]
	s_and_b64 s[20:21], s[0:1], vcc
	s_cmp_lg_u64 s[20:21], 0
	s_cselect_b32 s20, 4, 0
	s_or_b32 s76, s76, s20
	v_cmp_ne_u64_e32 vcc, -1, v[8:9]
	s_and_b64 s[20:21], s[0:1], vcc
	s_cmp_lg_u64 s[20:21], 0
	s_cselect_b32 s20, 4, 0
	s_or_b32 s77, s77, s20
	v_lshl_add_u64 v[4:5], v[4:5], 0, 8
	global_load_dword v172, v96, s[60:61] offset:2304 nt
	global_load_dword v173, v96, s[62:63] offset:2304 nt
	global_load_dword v174, v96, s[64:65] offset:2304 nt
	global_load_dword v175, v96, s[66:67] offset:2304 nt
	global_load_dword v176, v96, s[68:69] offset:2304 nt
	global_load_dword v177, v96, s[70:71] offset:2304 nt
	global_load_dword v178, v96, s[72:73] offset:2304 nt
	global_load_dword v179, v96, s[74:75] offset:2304 nt
	s_waitcnt vmcnt(51)
	v_cmp_ne_u32_e32 vcc, 0, v124
	s_nop 1
	v_mov_b32_e32 v2, vcc_lo
	v_mov_b32_e32 v9, vcc_hi
	v_cmp_ne_u32_e32 vcc, 0, v125
	v_cndmask_b32_e64 v2, 0, v2, s[22:23]
	v_cndmask_b32_e64 v9, 0, v9, s[22:23]
	v_mov_b32_e32 v11, vcc_hi
	v_mov_b32_e32 v14, vcc_lo
	v_cndmask_b32_e64 v9, v9, v11, s[6:7]
	v_cndmask_b32_e64 v2, v2, v14, s[6:7]
	v_cmp_ne_u32_e32 vcc, 0, v126
	s_nop 1
	v_mov_b32_e32 v11, vcc_lo
	v_mov_b32_e32 v14, vcc_hi
	v_cmp_ne_u32_e32 vcc, 0, v127
	v_cndmask_b32_e64 v2, v2, v11, s[8:9]
	v_cndmask_b32_e64 v9, v9, v14, s[8:9]
	v_mov_b32_e32 v11, vcc_hi
	v_mov_b32_e32 v14, vcc_lo
	v_cmp_ne_u32_e32 vcc, 0, v128
	v_cndmask_b32_e64 v9, v9, v11, s[10:11]
	v_cndmask_b32_e64 v2, v2, v14, s[10:11]
	v_mov_b32_e32 v11, vcc_lo
	v_mov_b32_e32 v12, vcc_hi
	v_cmp_ne_u32_e32 vcc, 0, v129
	v_cndmask_b32_e64 v2, v2, v11, s[12:13]
	v_cndmask_b32_e64 v9, v9, v12, s[12:13]
	v_mov_b32_e32 v11, vcc_hi
	v_mov_b32_e32 v12, vcc_lo
	v_cndmask_b32_e64 v9, v9, v11, s[14:15]
	v_cndmask_b32_e64 v2, v2, v12, s[14:15]
	v_cmp_ne_u32_e32 vcc, 0, v130
	s_nop 1
	v_mov_b32_e32 v10, vcc_lo
	v_mov_b32_e32 v11, vcc_hi
	v_cmp_ne_u32_e32 vcc, 0, v131
	v_cndmask_b32_e64 v2, v2, v10, s[16:17]
	v_cndmask_b32_e64 v8, v9, v11, s[16:17]
	v_mov_b32_e32 v9, vcc_hi
	v_mov_b32_e32 v10, vcc_lo
	v_cndmask_b32_e64 v9, v8, v9, s[18:19]
	v_cndmask_b32_e64 v8, v2, v10, s[18:19]
	s_mov_b64 s[2:3], exec
	s_mov_b64 exec, s[0:1]
	global_store_dwordx2 v[4:5], v[8:9], off
	s_mov_b64 exec, s[2:3]
	v_cmp_ne_u64_e32 vcc, 0, v[8:9]
	s_and_b64 s[20:21], s[0:1], vcc
	s_cmp_lg_u64 s[20:21], 0
	s_cselect_b32 s20, 8, 0
	s_or_b32 s76, s76, s20
	v_cmp_ne_u64_e32 vcc, -1, v[8:9]
	s_and_b64 s[20:21], s[0:1], vcc
	s_cmp_lg_u64 s[20:21], 0
	s_cselect_b32 s20, 8, 0
	s_or_b32 s77, s77, s20
	v_lshl_add_u64 v[4:5], v[4:5], 0, 8
	global_load_dword v180, v96, s[60:61] offset:2560 nt
	global_load_dword v181, v96, s[62:63] offset:2560 nt
	global_load_dword v182, v96, s[64:65] offset:2560 nt
	global_load_dword v183, v96, s[66:67] offset:2560 nt
	global_load_dword v184, v96, s[68:69] offset:2560 nt
	global_load_dword v185, v96, s[70:71] offset:2560 nt
	global_load_dword v186, v96, s[72:73] offset:2560 nt
	global_load_dword v187, v96, s[74:75] offset:2560 nt
	s_waitcnt vmcnt(52)
	v_cmp_ne_u32_e32 vcc, 0, v132
	s_nop 1
	v_mov_b32_e32 v2, vcc_lo
	v_mov_b32_e32 v9, vcc_hi
	v_cmp_ne_u32_e32 vcc, 0, v133
	v_cndmask_b32_e64 v2, 0, v2, s[22:23]
	v_cndmask_b32_e64 v9, 0, v9, s[22:23]
	v_mov_b32_e32 v11, vcc_hi
	v_mov_b32_e32 v14, vcc_lo
	v_cndmask_b32_e64 v9, v9, v11, s[6:7]
	v_cndmask_b32_e64 v2, v2, v14, s[6:7]
	v_cmp_ne_u32_e32 vcc, 0, v134
	s_nop 1
	v_mov_b32_e32 v11, vcc_lo
	v_mov_b32_e32 v14, vcc_hi
	v_cmp_ne_u32_e32 vcc, 0, v135
	v_cndmask_b32_e64 v2, v2, v11, s[8:9]
	v_cndmask_b32_e64 v9, v9, v14, s[8:9]
	v_mov_b32_e32 v11, vcc_hi
	v_mov_b32_e32 v14, vcc_lo
	v_cmp_ne_u32_e32 vcc, 0, v136
	v_cndmask_b32_e64 v9, v9, v11, s[10:11]
	v_cndmask_b32_e64 v2, v2, v14, s[10:11]
	v_mov_b32_e32 v11, vcc_lo
	v_mov_b32_e32 v12, vcc_hi
	v_cmp_ne_u32_e32 vcc, 0, v137
	v_cndmask_b32_e64 v2, v2, v11, s[12:13]
	v_cndmask_b32_e64 v9, v9, v12, s[12:13]
	v_mov_b32_e32 v11, vcc_hi
	v_mov_b32_e32 v12, vcc_lo
	v_cndmask_b32_e64 v9, v9, v11, s[14:15]
	v_cndmask_b32_e64 v2, v2, v12, s[14:15]
	v_cmp_ne_u32_e32 vcc, 0, v138
	s_nop 1
	v_mov_b32_e32 v10, vcc_lo
	v_mov_b32_e32 v11, vcc_hi
	v_cmp_ne_u32_e32 vcc, 0, v139
	v_cndmask_b32_e64 v2, v2, v10, s[16:17]
	v_cndmask_b32_e64 v8, v9, v11, s[16:17]
	v_mov_b32_e32 v9, vcc_hi
	v_mov_b32_e32 v10, vcc_lo
	v_cndmask_b32_e64 v9, v8, v9, s[18:19]
	v_cndmask_b32_e64 v8, v2, v10, s[18:19]
	s_mov_b64 s[2:3], exec
	s_mov_b64 exec, s[0:1]
	global_store_dwordx2 v[4:5], v[8:9], off
	s_mov_b64 exec, s[2:3]
	v_cmp_ne_u64_e32 vcc, 0, v[8:9]
	s_and_b64 s[20:21], s[0:1], vcc
	s_cmp_lg_u64 s[20:21], 0
	s_cselect_b32 s20, 16, 0
	s_or_b32 s76, s76, s20
	v_cmp_ne_u64_e32 vcc, -1, v[8:9]
	s_and_b64 s[20:21], s[0:1], vcc
	s_cmp_lg_u64 s[20:21], 0
	s_cselect_b32 s20, 16, 0
	s_or_b32 s77, s77, s20
	v_lshl_add_u64 v[4:5], v[4:5], 0, 8
	global_load_dword v188, v96, s[60:61] offset:2816 nt
	global_load_dword v189, v96, s[62:63] offset:2816 nt
	global_load_dword v190, v96, s[64:65] offset:2816 nt
	global_load_dword v191, v96, s[66:67] offset:2816 nt
	global_load_dword v192, v96, s[68:69] offset:2816 nt
	global_load_dword v193, v96, s[70:71] offset:2816 nt
	global_load_dword v194, v96, s[72:73] offset:2816 nt
	global_load_dword v195, v96, s[74:75] offset:2816 nt
	s_waitcnt vmcnt(53)
	v_cmp_ne_u32_e32 vcc, 0, v140
	s_nop 1
	v_mov_b32_e32 v2, vcc_lo
	v_mov_b32_e32 v9, vcc_hi
	v_cmp_ne_u32_e32 vcc, 0, v141
	v_cndmask_b32_e64 v2, 0, v2, s[22:23]
	v_cndmask_b32_e64 v9, 0, v9, s[22:23]
	v_mov_b32_e32 v11, vcc_hi
	v_mov_b32_e32 v14, vcc_lo
	v_cndmask_b32_e64 v9, v9, v11, s[6:7]
	v_cndmask_b32_e64 v2, v2, v14, s[6:7]
	v_cmp_ne_u32_e32 vcc, 0, v142
	s_nop 1
	v_mov_b32_e32 v11, vcc_lo
	v_mov_b32_e32 v14, vcc_hi
	v_cmp_ne_u32_e32 vcc, 0, v143
	v_cndmask_b32_e64 v2, v2, v11, s[8:9]
	v_cndmask_b32_e64 v9, v9, v14, s[8:9]
	v_mov_b32_e32 v11, vcc_hi
	v_mov_b32_e32 v14, vcc_lo
	v_cmp_ne_u32_e32 vcc, 0, v144
	v_cndmask_b32_e64 v9, v9, v11, s[10:11]
	v_cndmask_b32_e64 v2, v2, v14, s[10:11]
	v_mov_b32_e32 v11, vcc_lo
	v_mov_b32_e32 v12, vcc_hi
	v_cmp_ne_u32_e32 vcc, 0, v145
	v_cndmask_b32_e64 v2, v2, v11, s[12:13]
	v_cndmask_b32_e64 v9, v9, v12, s[12:13]
	v_mov_b32_e32 v11, vcc_hi
	v_mov_b32_e32 v12, vcc_lo
	v_cndmask_b32_e64 v9, v9, v11, s[14:15]
	v_cndmask_b32_e64 v2, v2, v12, s[14:15]
	v_cmp_ne_u32_e32 vcc, 0, v146
	s_nop 1
	v_mov_b32_e32 v10, vcc_lo
	v_mov_b32_e32 v11, vcc_hi
	v_cmp_ne_u32_e32 vcc, 0, v147
	v_cndmask_b32_e64 v2, v2, v10, s[16:17]
	v_cndmask_b32_e64 v8, v9, v11, s[16:17]
	v_mov_b32_e32 v9, vcc_hi
	v_mov_b32_e32 v10, vcc_lo
	v_cndmask_b32_e64 v9, v8, v9, s[18:19]
	v_cndmask_b32_e64 v8, v2, v10, s[18:19]
	s_mov_b64 s[2:3], exec
	s_mov_b64 exec, s[0:1]
	global_store_dwordx2 v[4:5], v[8:9], off
	s_mov_b64 exec, s[2:3]
	v_cmp_ne_u64_e32 vcc, 0, v[8:9]
	s_and_b64 s[20:21], s[0:1], vcc
	s_cmp_lg_u64 s[20:21], 0
	s_cselect_b32 s20, 32, 0
	s_or_b32 s76, s76, s20
	v_cmp_ne_u64_e32 vcc, -1, v[8:9]
	s_and_b64 s[20:21], s[0:1], vcc
	s_cmp_lg_u64 s[20:21], 0
	s_cselect_b32 s20, 32, 0
	s_or_b32 s77, s77, s20
	v_lshl_add_u64 v[4:5], v[4:5], 0, 8
	global_load_dword v196, v96, s[60:61] offset:3072 nt
	global_load_dword v197, v96, s[62:63] offset:3072 nt
	global_load_dword v198, v96, s[64:65] offset:3072 nt
	global_load_dword v199, v96, s[66:67] offset:3072 nt
	global_load_dword v200, v96, s[68:69] offset:3072 nt
	global_load_dword v201, v96, s[70:71] offset:3072 nt
	global_load_dword v202, v96, s[72:73] offset:3072 nt
	global_load_dword v203, v96, s[74:75] offset:3072 nt
	s_waitcnt vmcnt(54)
	v_cmp_ne_u32_e32 vcc, 0, v148
	s_nop 1
	v_mov_b32_e32 v2, vcc_lo
	v_mov_b32_e32 v9, vcc_hi
	v_cmp_ne_u32_e32 vcc, 0, v149
	v_cndmask_b32_e64 v2, 0, v2, s[22:23]
	v_cndmask_b32_e64 v9, 0, v9, s[22:23]
	v_mov_b32_e32 v11, vcc_hi
	v_mov_b32_e32 v14, vcc_lo
	v_cndmask_b32_e64 v9, v9, v11, s[6:7]
	v_cndmask_b32_e64 v2, v2, v14, s[6:7]
	v_cmp_ne_u32_e32 vcc, 0, v150
	s_nop 1
	v_mov_b32_e32 v11, vcc_lo
	v_mov_b32_e32 v14, vcc_hi
	v_cmp_ne_u32_e32 vcc, 0, v151
	v_cndmask_b32_e64 v2, v2, v11, s[8:9]
	v_cndmask_b32_e64 v9, v9, v14, s[8:9]
	v_mov_b32_e32 v11, vcc_hi
	v_mov_b32_e32 v14, vcc_lo
	v_cmp_ne_u32_e32 vcc, 0, v152
	v_cndmask_b32_e64 v9, v9, v11, s[10:11]
	v_cndmask_b32_e64 v2, v2, v14, s[10:11]
	v_mov_b32_e32 v11, vcc_lo
	v_mov_b32_e32 v12, vcc_hi
	v_cmp_ne_u32_e32 vcc, 0, v153
	v_cndmask_b32_e64 v2, v2, v11, s[12:13]
	v_cndmask_b32_e64 v9, v9, v12, s[12:13]
	v_mov_b32_e32 v11, vcc_hi
	v_mov_b32_e32 v12, vcc_lo
	v_cndmask_b32_e64 v9, v9, v11, s[14:15]
	v_cndmask_b32_e64 v2, v2, v12, s[14:15]
	v_cmp_ne_u32_e32 vcc, 0, v154
	s_nop 1
	v_mov_b32_e32 v10, vcc_lo
	v_mov_b32_e32 v11, vcc_hi
	v_cmp_ne_u32_e32 vcc, 0, v155
	v_cndmask_b32_e64 v2, v2, v10, s[16:17]
	v_cndmask_b32_e64 v8, v9, v11, s[16:17]
	v_mov_b32_e32 v9, vcc_hi
	v_mov_b32_e32 v10, vcc_lo
	v_cndmask_b32_e64 v9, v8, v9, s[18:19]
	v_cndmask_b32_e64 v8, v2, v10, s[18:19]
	s_mov_b64 s[2:3], exec
	s_mov_b64 exec, s[0:1]
	global_store_dwordx2 v[4:5], v[8:9], off
	s_mov_b64 exec, s[2:3]
	v_cmp_ne_u64_e32 vcc, 0, v[8:9]
	s_and_b64 s[20:21], s[0:1], vcc
	s_cmp_lg_u64 s[20:21], 0
	s_cselect_b32 s20, 64, 0
	s_or_b32 s76, s76, s20
	v_cmp_ne_u64_e32 vcc, -1, v[8:9]
	s_and_b64 s[20:21], s[0:1], vcc
	s_cmp_lg_u64 s[20:21], 0
	s_cselect_b32 s20, 64, 0
	s_or_b32 s77, s77, s20
	v_lshl_add_u64 v[4:5], v[4:5], 0, 8
	global_load_dword v204, v96, s[60:61] offset:3328 nt
	global_load_dword v205, v96, s[62:63] offset:3328 nt
	global_load_dword v206, v96, s[64:65] offset:3328 nt
	global_load_dword v207, v96, s[66:67] offset:3328 nt
	global_load_dword v208, v96, s[68:69] offset:3328 nt
	global_load_dword v209, v96, s[70:71] offset:3328 nt
	global_load_dword v210, v96, s[72:73] offset:3328 nt
	global_load_dword v211, v96, s[74:75] offset:3328 nt
	s_waitcnt vmcnt(54)
	v_cmp_ne_u32_e32 vcc, 0, v156
	s_nop 1
	v_mov_b32_e32 v2, vcc_lo
	v_mov_b32_e32 v9, vcc_hi
	v_cmp_ne_u32_e32 vcc, 0, v157
	v_cndmask_b32_e64 v2, 0, v2, s[22:23]
	v_cndmask_b32_e64 v9, 0, v9, s[22:23]
	v_mov_b32_e32 v11, vcc_hi
	v_mov_b32_e32 v14, vcc_lo
	v_cndmask_b32_e64 v9, v9, v11, s[6:7]
	v_cndmask_b32_e64 v2, v2, v14, s[6:7]
	v_cmp_ne_u32_e32 vcc, 0, v158
	s_nop 1
	v_mov_b32_e32 v11, vcc_lo
	v_mov_b32_e32 v14, vcc_hi
	v_cmp_ne_u32_e32 vcc, 0, v159
	v_cndmask_b32_e64 v2, v2, v11, s[8:9]
	v_cndmask_b32_e64 v9, v9, v14, s[8:9]
	v_mov_b32_e32 v11, vcc_hi
	v_mov_b32_e32 v14, vcc_lo
	v_cmp_ne_u32_e32 vcc, 0, v160
	v_cndmask_b32_e64 v9, v9, v11, s[10:11]
	v_cndmask_b32_e64 v2, v2, v14, s[10:11]
	v_mov_b32_e32 v11, vcc_lo
	v_mov_b32_e32 v12, vcc_hi
	v_cmp_ne_u32_e32 vcc, 0, v161
	v_cndmask_b32_e64 v2, v2, v11, s[12:13]
	v_cndmask_b32_e64 v9, v9, v12, s[12:13]
	v_mov_b32_e32 v11, vcc_hi
	v_mov_b32_e32 v12, vcc_lo
	v_cndmask_b32_e64 v9, v9, v11, s[14:15]
	v_cndmask_b32_e64 v2, v2, v12, s[14:15]
	v_cmp_ne_u32_e32 vcc, 0, v162
	s_nop 1
	v_mov_b32_e32 v10, vcc_lo
	v_mov_b32_e32 v11, vcc_hi
	v_cmp_ne_u32_e32 vcc, 0, v163
	v_cndmask_b32_e64 v2, v2, v10, s[16:17]
	v_cndmask_b32_e64 v8, v9, v11, s[16:17]
	v_mov_b32_e32 v9, vcc_hi
	v_mov_b32_e32 v10, vcc_lo
	v_cndmask_b32_e64 v9, v8, v9, s[18:19]
	v_cndmask_b32_e64 v8, v2, v10, s[18:19]
	s_mov_b64 s[2:3], exec
	s_mov_b64 exec, s[0:1]
	global_store_dwordx2 v[4:5], v[8:9], off
	s_mov_b64 exec, s[2:3]
	v_cmp_ne_u64_e32 vcc, 0, v[8:9]
	s_and_b64 s[20:21], s[0:1], vcc
	s_cmp_lg_u64 s[20:21], 0
	s_cselect_b32 s20, 128, 0
	s_or_b32 s76, s76, s20
	v_cmp_ne_u64_e32 vcc, -1, v[8:9]
	s_and_b64 s[20:21], s[0:1], vcc
	s_cmp_lg_u64 s[20:21], 0
	s_cselect_b32 s20, 128, 0
	s_or_b32 s77, s77, s20
	v_lshl_add_u64 v[4:5], v[4:5], 0, 8
	global_load_dword v212, v96, s[60:61] offset:3584 nt
	global_load_dword v213, v96, s[62:63] offset:3584 nt
	global_load_dword v214, v96, s[64:65] offset:3584 nt
	global_load_dword v215, v96, s[66:67] offset:3584 nt
	global_load_dword v216, v96, s[68:69] offset:3584 nt
	global_load_dword v217, v96, s[70:71] offset:3584 nt
	global_load_dword v218, v96, s[72:73] offset:3584 nt
	global_load_dword v219, v96, s[74:75] offset:3584 nt
	s_waitcnt vmcnt(54)
	v_cmp_ne_u32_e32 vcc, 0, v164
	s_nop 1
	v_mov_b32_e32 v2, vcc_lo
	v_mov_b32_e32 v9, vcc_hi
	v_cmp_ne_u32_e32 vcc, 0, v165
	v_cndmask_b32_e64 v2, 0, v2, s[22:23]
	v_cndmask_b32_e64 v9, 0, v9, s[22:23]
	v_mov_b32_e32 v11, vcc_hi
	v_mov_b32_e32 v14, vcc_lo
	v_cndmask_b32_e64 v9, v9, v11, s[6:7]
	v_cndmask_b32_e64 v2, v2, v14, s[6:7]
	v_cmp_ne_u32_e32 vcc, 0, v166
	s_nop 1
	v_mov_b32_e32 v11, vcc_lo
	v_mov_b32_e32 v14, vcc_hi
	v_cmp_ne_u32_e32 vcc, 0, v167
	v_cndmask_b32_e64 v2, v2, v11, s[8:9]
	v_cndmask_b32_e64 v9, v9, v14, s[8:9]
	v_mov_b32_e32 v11, vcc_hi
	v_mov_b32_e32 v14, vcc_lo
	v_cmp_ne_u32_e32 vcc, 0, v168
	v_cndmask_b32_e64 v9, v9, v11, s[10:11]
	v_cndmask_b32_e64 v2, v2, v14, s[10:11]
	v_mov_b32_e32 v11, vcc_lo
	v_mov_b32_e32 v12, vcc_hi
	v_cmp_ne_u32_e32 vcc, 0, v169
	v_cndmask_b32_e64 v2, v2, v11, s[12:13]
	v_cndmask_b32_e64 v9, v9, v12, s[12:13]
	v_mov_b32_e32 v11, vcc_hi
	v_mov_b32_e32 v12, vcc_lo
	v_cndmask_b32_e64 v9, v9, v11, s[14:15]
	v_cndmask_b32_e64 v2, v2, v12, s[14:15]
	v_cmp_ne_u32_e32 vcc, 0, v170
	s_nop 1
	v_mov_b32_e32 v10, vcc_lo
	v_mov_b32_e32 v11, vcc_hi
	v_cmp_ne_u32_e32 vcc, 0, v171
	v_cndmask_b32_e64 v2, v2, v10, s[16:17]
	v_cndmask_b32_e64 v8, v9, v11, s[16:17]
	v_mov_b32_e32 v9, vcc_hi
	v_mov_b32_e32 v10, vcc_lo
	v_cndmask_b32_e64 v9, v8, v9, s[18:19]
	v_cndmask_b32_e64 v8, v2, v10, s[18:19]
	s_mov_b64 s[2:3], exec
	s_mov_b64 exec, s[0:1]
	global_store_dwordx2 v[4:5], v[8:9], off
	s_mov_b64 exec, s[2:3]
	v_cmp_ne_u64_e32 vcc, 0, v[8:9]
	s_and_b64 s[20:21], s[0:1], vcc
	s_cmp_lg_u64 s[20:21], 0
	s_cselect_b32 s20, 256, 0
	s_or_b32 s76, s76, s20
	v_cmp_ne_u64_e32 vcc, -1, v[8:9]
	s_and_b64 s[20:21], s[0:1], vcc
	s_cmp_lg_u64 s[20:21], 0
	s_cselect_b32 s20, 256, 0
	s_or_b32 s77, s77, s20
	v_lshl_add_u64 v[4:5], v[4:5], 0, 8
	global_load_dword v220, v96, s[60:61] offset:3840 nt
	global_load_dword v221, v96, s[62:63] offset:3840 nt
	global_load_dword v222, v96, s[64:65] offset:3840 nt
	global_load_dword v223, v96, s[66:67] offset:3840 nt
	global_load_dword v224, v96, s[68:69] offset:3840 nt
	global_load_dword v225, v96, s[70:71] offset:3840 nt
	global_load_dword v226, v96, s[72:73] offset:3840 nt
	global_load_dword v227, v96, s[74:75] offset:3840 nt
	s_waitcnt vmcnt(54)
	v_cmp_ne_u32_e32 vcc, 0, v172
	s_nop 1
	v_mov_b32_e32 v2, vcc_lo
	v_mov_b32_e32 v9, vcc_hi
	v_cmp_ne_u32_e32 vcc, 0, v173
	v_cndmask_b32_e64 v2, 0, v2, s[22:23]
	v_cndmask_b32_e64 v9, 0, v9, s[22:23]
	v_mov_b32_e32 v11, vcc_hi
	v_mov_b32_e32 v14, vcc_lo
	v_cndmask_b32_e64 v9, v9, v11, s[6:7]
	v_cndmask_b32_e64 v2, v2, v14, s[6:7]
	v_cmp_ne_u32_e32 vcc, 0, v174
	s_nop 1
	v_mov_b32_e32 v11, vcc_lo
	v_mov_b32_e32 v14, vcc_hi
	v_cmp_ne_u32_e32 vcc, 0, v175
	v_cndmask_b32_e64 v2, v2, v11, s[8:9]
	v_cndmask_b32_e64 v9, v9, v14, s[8:9]
	v_mov_b32_e32 v11, vcc_hi
	v_mov_b32_e32 v14, vcc_lo
	v_cmp_ne_u32_e32 vcc, 0, v176
	v_cndmask_b32_e64 v9, v9, v11, s[10:11]
	v_cndmask_b32_e64 v2, v2, v14, s[10:11]
	v_mov_b32_e32 v11, vcc_lo
	v_mov_b32_e32 v12, vcc_hi
	v_cmp_ne_u32_e32 vcc, 0, v177
	v_cndmask_b32_e64 v2, v2, v11, s[12:13]
	v_cndmask_b32_e64 v9, v9, v12, s[12:13]
	v_mov_b32_e32 v11, vcc_hi
	v_mov_b32_e32 v12, vcc_lo
	v_cndmask_b32_e64 v9, v9, v11, s[14:15]
	v_cndmask_b32_e64 v2, v2, v12, s[14:15]
	v_cmp_ne_u32_e32 vcc, 0, v178
	s_nop 1
	v_mov_b32_e32 v10, vcc_lo
	v_mov_b32_e32 v11, vcc_hi
	v_cmp_ne_u32_e32 vcc, 0, v179
	v_cndmask_b32_e64 v2, v2, v10, s[16:17]
	v_cndmask_b32_e64 v8, v9, v11, s[16:17]
	v_mov_b32_e32 v9, vcc_hi
	v_mov_b32_e32 v10, vcc_lo
	v_cndmask_b32_e64 v9, v8, v9, s[18:19]
	v_cndmask_b32_e64 v8, v2, v10, s[18:19]
	s_mov_b64 s[2:3], exec
	s_mov_b64 exec, s[0:1]
	global_store_dwordx2 v[4:5], v[8:9], off
	s_mov_b64 exec, s[2:3]
	v_cmp_ne_u64_e32 vcc, 0, v[8:9]
	s_and_b64 s[20:21], s[0:1], vcc
	s_cmp_lg_u64 s[20:21], 0
	s_cselect_b32 s20, 512, 0
	s_or_b32 s76, s76, s20
	v_cmp_ne_u64_e32 vcc, -1, v[8:9]
	s_and_b64 s[20:21], s[0:1], vcc
	s_cmp_lg_u64 s[20:21], 0
	s_cselect_b32 s20, 512, 0
	s_or_b32 s77, s77, s20
	v_lshl_add_u64 v[4:5], v[4:5], 0, 8
	s_waitcnt vmcnt(46)
	v_cmp_ne_u32_e32 vcc, 0, v180
	s_nop 1
	v_mov_b32_e32 v2, vcc_lo
	v_mov_b32_e32 v9, vcc_hi
	v_cmp_ne_u32_e32 vcc, 0, v181
	v_cndmask_b32_e64 v2, 0, v2, s[22:23]
	v_cndmask_b32_e64 v9, 0, v9, s[22:23]
	v_mov_b32_e32 v11, vcc_hi
	v_mov_b32_e32 v14, vcc_lo
	v_cndmask_b32_e64 v9, v9, v11, s[6:7]
	v_cndmask_b32_e64 v2, v2, v14, s[6:7]
	v_cmp_ne_u32_e32 vcc, 0, v182
	s_nop 1
	v_mov_b32_e32 v11, vcc_lo
	v_mov_b32_e32 v14, vcc_hi
	v_cmp_ne_u32_e32 vcc, 0, v183
	v_cndmask_b32_e64 v2, v2, v11, s[8:9]
	v_cndmask_b32_e64 v9, v9, v14, s[8:9]
	v_mov_b32_e32 v11, vcc_hi
	v_mov_b32_e32 v14, vcc_lo
	v_cmp_ne_u32_e32 vcc, 0, v184
	v_cndmask_b32_e64 v9, v9, v11, s[10:11]
	v_cndmask_b32_e64 v2, v2, v14, s[10:11]
	v_mov_b32_e32 v11, vcc_lo
	v_mov_b32_e32 v12, vcc_hi
	v_cmp_ne_u32_e32 vcc, 0, v185
	v_cndmask_b32_e64 v2, v2, v11, s[12:13]
	v_cndmask_b32_e64 v9, v9, v12, s[12:13]
	v_mov_b32_e32 v11, vcc_hi
	v_mov_b32_e32 v12, vcc_lo
	v_cndmask_b32_e64 v9, v9, v11, s[14:15]
	v_cndmask_b32_e64 v2, v2, v12, s[14:15]
	v_cmp_ne_u32_e32 vcc, 0, v186
	s_nop 1
	v_mov_b32_e32 v10, vcc_lo
	v_mov_b32_e32 v11, vcc_hi
	v_cmp_ne_u32_e32 vcc, 0, v187
	v_cndmask_b32_e64 v2, v2, v10, s[16:17]
	v_cndmask_b32_e64 v8, v9, v11, s[16:17]
	v_mov_b32_e32 v9, vcc_hi
	v_mov_b32_e32 v10, vcc_lo
	v_cndmask_b32_e64 v9, v8, v9, s[18:19]
	v_cndmask_b32_e64 v8, v2, v10, s[18:19]
	s_mov_b64 s[2:3], exec
	s_mov_b64 exec, s[0:1]
	global_store_dwordx2 v[4:5], v[8:9], off
	s_mov_b64 exec, s[2:3]
	v_cmp_ne_u64_e32 vcc, 0, v[8:9]
	s_and_b64 s[20:21], s[0:1], vcc
	s_cmp_lg_u64 s[20:21], 0
	s_cselect_b32 s20, 1024, 0
	s_or_b32 s76, s76, s20
	v_cmp_ne_u64_e32 vcc, -1, v[8:9]
	s_and_b64 s[20:21], s[0:1], vcc
	s_cmp_lg_u64 s[20:21], 0
	s_cselect_b32 s20, 1024, 0
	s_or_b32 s77, s77, s20
	v_lshl_add_u64 v[4:5], v[4:5], 0, 8
	s_waitcnt vmcnt(38)
	v_cmp_ne_u32_e32 vcc, 0, v188
	s_nop 1
	v_mov_b32_e32 v2, vcc_lo
	v_mov_b32_e32 v9, vcc_hi
	v_cmp_ne_u32_e32 vcc, 0, v189
	v_cndmask_b32_e64 v2, 0, v2, s[22:23]
	v_cndmask_b32_e64 v9, 0, v9, s[22:23]
	v_mov_b32_e32 v11, vcc_hi
	v_mov_b32_e32 v14, vcc_lo
	v_cndmask_b32_e64 v9, v9, v11, s[6:7]
	v_cndmask_b32_e64 v2, v2, v14, s[6:7]
	v_cmp_ne_u32_e32 vcc, 0, v190
	s_nop 1
	v_mov_b32_e32 v11, vcc_lo
	v_mov_b32_e32 v14, vcc_hi
	v_cmp_ne_u32_e32 vcc, 0, v191
	v_cndmask_b32_e64 v2, v2, v11, s[8:9]
	v_cndmask_b32_e64 v9, v9, v14, s[8:9]
	v_mov_b32_e32 v11, vcc_hi
	v_mov_b32_e32 v14, vcc_lo
	v_cmp_ne_u32_e32 vcc, 0, v192
	v_cndmask_b32_e64 v9, v9, v11, s[10:11]
	v_cndmask_b32_e64 v2, v2, v14, s[10:11]
	v_mov_b32_e32 v11, vcc_lo
	v_mov_b32_e32 v12, vcc_hi
	v_cmp_ne_u32_e32 vcc, 0, v193
	v_cndmask_b32_e64 v2, v2, v11, s[12:13]
	v_cndmask_b32_e64 v9, v9, v12, s[12:13]
	v_mov_b32_e32 v11, vcc_hi
	v_mov_b32_e32 v12, vcc_lo
	v_cndmask_b32_e64 v9, v9, v11, s[14:15]
	v_cndmask_b32_e64 v2, v2, v12, s[14:15]
	v_cmp_ne_u32_e32 vcc, 0, v194
	s_nop 1
	v_mov_b32_e32 v10, vcc_lo
	v_mov_b32_e32 v11, vcc_hi
	v_cmp_ne_u32_e32 vcc, 0, v195
	v_cndmask_b32_e64 v2, v2, v10, s[16:17]
	v_cndmask_b32_e64 v8, v9, v11, s[16:17]
	v_mov_b32_e32 v9, vcc_hi
	v_mov_b32_e32 v10, vcc_lo
	v_cndmask_b32_e64 v9, v8, v9, s[18:19]
	v_cndmask_b32_e64 v8, v2, v10, s[18:19]
	s_mov_b64 s[2:3], exec
	s_mov_b64 exec, s[0:1]
	global_store_dwordx2 v[4:5], v[8:9], off
	s_mov_b64 exec, s[2:3]
	v_cmp_ne_u64_e32 vcc, 0, v[8:9]
	s_and_b64 s[20:21], s[0:1], vcc
	s_cmp_lg_u64 s[20:21], 0
	s_cselect_b32 s20, 2048, 0
	s_or_b32 s76, s76, s20
	v_cmp_ne_u64_e32 vcc, -1, v[8:9]
	s_and_b64 s[20:21], s[0:1], vcc
	s_cmp_lg_u64 s[20:21], 0
	s_cselect_b32 s20, 2048, 0
	s_or_b32 s77, s77, s20
	v_lshl_add_u64 v[4:5], v[4:5], 0, 8
	s_waitcnt vmcnt(30)
	v_cmp_ne_u32_e32 vcc, 0, v196
	s_nop 1
	v_mov_b32_e32 v2, vcc_lo
	v_mov_b32_e32 v9, vcc_hi
	v_cmp_ne_u32_e32 vcc, 0, v197
	v_cndmask_b32_e64 v2, 0, v2, s[22:23]
	v_cndmask_b32_e64 v9, 0, v9, s[22:23]
	v_mov_b32_e32 v11, vcc_hi
	v_mov_b32_e32 v14, vcc_lo
	v_cndmask_b32_e64 v9, v9, v11, s[6:7]
	v_cndmask_b32_e64 v2, v2, v14, s[6:7]
	v_cmp_ne_u32_e32 vcc, 0, v198
	s_nop 1
	v_mov_b32_e32 v11, vcc_lo
	v_mov_b32_e32 v14, vcc_hi
	v_cmp_ne_u32_e32 vcc, 0, v199
	v_cndmask_b32_e64 v2, v2, v11, s[8:9]
	v_cndmask_b32_e64 v9, v9, v14, s[8:9]
	v_mov_b32_e32 v11, vcc_hi
	v_mov_b32_e32 v14, vcc_lo
	v_cmp_ne_u32_e32 vcc, 0, v200
	v_cndmask_b32_e64 v9, v9, v11, s[10:11]
	v_cndmask_b32_e64 v2, v2, v14, s[10:11]
	v_mov_b32_e32 v11, vcc_lo
	v_mov_b32_e32 v12, vcc_hi
	v_cmp_ne_u32_e32 vcc, 0, v201
	v_cndmask_b32_e64 v2, v2, v11, s[12:13]
	v_cndmask_b32_e64 v9, v9, v12, s[12:13]
	v_mov_b32_e32 v11, vcc_hi
	v_mov_b32_e32 v12, vcc_lo
	v_cndmask_b32_e64 v9, v9, v11, s[14:15]
	v_cndmask_b32_e64 v2, v2, v12, s[14:15]
	v_cmp_ne_u32_e32 vcc, 0, v202
	s_nop 1
	v_mov_b32_e32 v10, vcc_lo
	v_mov_b32_e32 v11, vcc_hi
	v_cmp_ne_u32_e32 vcc, 0, v203
	v_cndmask_b32_e64 v2, v2, v10, s[16:17]
	v_cndmask_b32_e64 v8, v9, v11, s[16:17]
	v_mov_b32_e32 v9, vcc_hi
	v_mov_b32_e32 v10, vcc_lo
	v_cndmask_b32_e64 v9, v8, v9, s[18:19]
	v_cndmask_b32_e64 v8, v2, v10, s[18:19]
	s_mov_b64 s[2:3], exec
	s_mov_b64 exec, s[0:1]
	global_store_dwordx2 v[4:5], v[8:9], off
	s_mov_b64 exec, s[2:3]
	v_cmp_ne_u64_e32 vcc, 0, v[8:9]
	s_and_b64 s[20:21], s[0:1], vcc
	s_cmp_lg_u64 s[20:21], 0
	s_cselect_b32 s20, 4096, 0
	s_or_b32 s76, s76, s20
	v_cmp_ne_u64_e32 vcc, -1, v[8:9]
	s_and_b64 s[20:21], s[0:1], vcc
	s_cmp_lg_u64 s[20:21], 0
	s_cselect_b32 s20, 4096, 0
	s_or_b32 s77, s77, s20
	v_lshl_add_u64 v[4:5], v[4:5], 0, 8
	s_waitcnt vmcnt(22)
	v_cmp_ne_u32_e32 vcc, 0, v204
	s_nop 1
	v_mov_b32_e32 v2, vcc_lo
	v_mov_b32_e32 v9, vcc_hi
	v_cmp_ne_u32_e32 vcc, 0, v205
	v_cndmask_b32_e64 v2, 0, v2, s[22:23]
	v_cndmask_b32_e64 v9, 0, v9, s[22:23]
	v_mov_b32_e32 v11, vcc_hi
	v_mov_b32_e32 v14, vcc_lo
	v_cndmask_b32_e64 v9, v9, v11, s[6:7]
	v_cndmask_b32_e64 v2, v2, v14, s[6:7]
	v_cmp_ne_u32_e32 vcc, 0, v206
	s_nop 1
	v_mov_b32_e32 v11, vcc_lo
	v_mov_b32_e32 v14, vcc_hi
	v_cmp_ne_u32_e32 vcc, 0, v207
	v_cndmask_b32_e64 v2, v2, v11, s[8:9]
	v_cndmask_b32_e64 v9, v9, v14, s[8:9]
	v_mov_b32_e32 v11, vcc_hi
	v_mov_b32_e32 v14, vcc_lo
	v_cmp_ne_u32_e32 vcc, 0, v208
	v_cndmask_b32_e64 v9, v9, v11, s[10:11]
	v_cndmask_b32_e64 v2, v2, v14, s[10:11]
	v_mov_b32_e32 v11, vcc_lo
	v_mov_b32_e32 v12, vcc_hi
	v_cmp_ne_u32_e32 vcc, 0, v209
	v_cndmask_b32_e64 v2, v2, v11, s[12:13]
	v_cndmask_b32_e64 v9, v9, v12, s[12:13]
	v_mov_b32_e32 v11, vcc_hi
	v_mov_b32_e32 v12, vcc_lo
	v_cndmask_b32_e64 v9, v9, v11, s[14:15]
	v_cndmask_b32_e64 v2, v2, v12, s[14:15]
	v_cmp_ne_u32_e32 vcc, 0, v210
	s_nop 1
	v_mov_b32_e32 v10, vcc_lo
	v_mov_b32_e32 v11, vcc_hi
	v_cmp_ne_u32_e32 vcc, 0, v211
	v_cndmask_b32_e64 v2, v2, v10, s[16:17]
	v_cndmask_b32_e64 v8, v9, v11, s[16:17]
	v_mov_b32_e32 v9, vcc_hi
	v_mov_b32_e32 v10, vcc_lo
	v_cndmask_b32_e64 v9, v8, v9, s[18:19]
	v_cndmask_b32_e64 v8, v2, v10, s[18:19]
	s_mov_b64 s[2:3], exec
	s_mov_b64 exec, s[0:1]
	global_store_dwordx2 v[4:5], v[8:9], off
	s_mov_b64 exec, s[2:3]
	v_cmp_ne_u64_e32 vcc, 0, v[8:9]
	s_and_b64 s[20:21], s[0:1], vcc
	s_cmp_lg_u64 s[20:21], 0
	s_cselect_b32 s20, 8192, 0
	s_or_b32 s76, s76, s20
	v_cmp_ne_u64_e32 vcc, -1, v[8:9]
	s_and_b64 s[20:21], s[0:1], vcc
	s_cmp_lg_u64 s[20:21], 0
	s_cselect_b32 s20, 8192, 0
	s_or_b32 s77, s77, s20
	v_lshl_add_u64 v[4:5], v[4:5], 0, 8
	s_waitcnt vmcnt(14)
	v_cmp_ne_u32_e32 vcc, 0, v212
	s_nop 1
	v_mov_b32_e32 v2, vcc_lo
	v_mov_b32_e32 v9, vcc_hi
	v_cmp_ne_u32_e32 vcc, 0, v213
	v_cndmask_b32_e64 v2, 0, v2, s[22:23]
	v_cndmask_b32_e64 v9, 0, v9, s[22:23]
	v_mov_b32_e32 v11, vcc_hi
	v_mov_b32_e32 v14, vcc_lo
	v_cndmask_b32_e64 v9, v9, v11, s[6:7]
	v_cndmask_b32_e64 v2, v2, v14, s[6:7]
	v_cmp_ne_u32_e32 vcc, 0, v214
	s_nop 1
	v_mov_b32_e32 v11, vcc_lo
	v_mov_b32_e32 v14, vcc_hi
	v_cmp_ne_u32_e32 vcc, 0, v215
	v_cndmask_b32_e64 v2, v2, v11, s[8:9]
	v_cndmask_b32_e64 v9, v9, v14, s[8:9]
	v_mov_b32_e32 v11, vcc_hi
	v_mov_b32_e32 v14, vcc_lo
	v_cmp_ne_u32_e32 vcc, 0, v216
	v_cndmask_b32_e64 v9, v9, v11, s[10:11]
	v_cndmask_b32_e64 v2, v2, v14, s[10:11]
	v_mov_b32_e32 v11, vcc_lo
	v_mov_b32_e32 v12, vcc_hi
	v_cmp_ne_u32_e32 vcc, 0, v217
	v_cndmask_b32_e64 v2, v2, v11, s[12:13]
	v_cndmask_b32_e64 v9, v9, v12, s[12:13]
	v_mov_b32_e32 v11, vcc_hi
	v_mov_b32_e32 v12, vcc_lo
	v_cndmask_b32_e64 v9, v9, v11, s[14:15]
	v_cndmask_b32_e64 v2, v2, v12, s[14:15]
	v_cmp_ne_u32_e32 vcc, 0, v218
	s_nop 1
	v_mov_b32_e32 v10, vcc_lo
	v_mov_b32_e32 v11, vcc_hi
	v_cmp_ne_u32_e32 vcc, 0, v219
	v_cndmask_b32_e64 v2, v2, v10, s[16:17]
	v_cndmask_b32_e64 v8, v9, v11, s[16:17]
	v_mov_b32_e32 v9, vcc_hi
	v_mov_b32_e32 v10, vcc_lo
	v_cndmask_b32_e64 v9, v8, v9, s[18:19]
	v_cndmask_b32_e64 v8, v2, v10, s[18:19]
	s_mov_b64 s[2:3], exec
	s_mov_b64 exec, s[0:1]
	global_store_dwordx2 v[4:5], v[8:9], off
	s_mov_b64 exec, s[2:3]
	v_cmp_ne_u64_e32 vcc, 0, v[8:9]
	s_and_b64 s[20:21], s[0:1], vcc
	s_cmp_lg_u64 s[20:21], 0
	s_cselect_b32 s20, 16384, 0
	s_or_b32 s76, s76, s20
	v_cmp_ne_u64_e32 vcc, -1, v[8:9]
	s_and_b64 s[20:21], s[0:1], vcc
	s_cmp_lg_u64 s[20:21], 0
	s_cselect_b32 s20, 16384, 0
	s_or_b32 s77, s77, s20
	v_lshl_add_u64 v[4:5], v[4:5], 0, 8
	s_waitcnt vmcnt(6)
	v_cmp_ne_u32_e32 vcc, 0, v220
	s_nop 1
	v_mov_b32_e32 v2, vcc_lo
	v_mov_b32_e32 v9, vcc_hi
	v_cmp_ne_u32_e32 vcc, 0, v221
	v_cndmask_b32_e64 v2, 0, v2, s[22:23]
	v_cndmask_b32_e64 v9, 0, v9, s[22:23]
	v_mov_b32_e32 v11, vcc_hi
	v_mov_b32_e32 v14, vcc_lo
	v_cndmask_b32_e64 v9, v9, v11, s[6:7]
	v_cndmask_b32_e64 v2, v2, v14, s[6:7]
	v_cmp_ne_u32_e32 vcc, 0, v222
	s_nop 1
	v_mov_b32_e32 v11, vcc_lo
	v_mov_b32_e32 v14, vcc_hi
	v_cmp_ne_u32_e32 vcc, 0, v223
	v_cndmask_b32_e64 v2, v2, v11, s[8:9]
	v_cndmask_b32_e64 v9, v9, v14, s[8:9]
	v_mov_b32_e32 v11, vcc_hi
	v_mov_b32_e32 v14, vcc_lo
	v_cmp_ne_u32_e32 vcc, 0, v224
	v_cndmask_b32_e64 v9, v9, v11, s[10:11]
	v_cndmask_b32_e64 v2, v2, v14, s[10:11]
	v_mov_b32_e32 v11, vcc_lo
	v_mov_b32_e32 v12, vcc_hi
	v_cmp_ne_u32_e32 vcc, 0, v225
	v_cndmask_b32_e64 v2, v2, v11, s[12:13]
	v_cndmask_b32_e64 v9, v9, v12, s[12:13]
	v_mov_b32_e32 v11, vcc_hi
	v_mov_b32_e32 v12, vcc_lo
	v_cndmask_b32_e64 v9, v9, v11, s[14:15]
	v_cndmask_b32_e64 v2, v2, v12, s[14:15]
	v_cmp_ne_u32_e32 vcc, 0, v226
	s_nop 1
	v_mov_b32_e32 v10, vcc_lo
	v_mov_b32_e32 v11, vcc_hi
	v_cmp_ne_u32_e32 vcc, 0, v227
	v_cndmask_b32_e64 v2, v2, v10, s[16:17]
	v_cndmask_b32_e64 v8, v9, v11, s[16:17]
	v_mov_b32_e32 v9, vcc_hi
	v_mov_b32_e32 v10, vcc_lo
	v_cndmask_b32_e64 v9, v8, v9, s[18:19]
	v_cndmask_b32_e64 v8, v2, v10, s[18:19]
	s_mov_b64 s[2:3], exec
	s_mov_b64 exec, s[0:1]
	global_store_dwordx2 v[4:5], v[8:9], off
	s_mov_b64 exec, s[2:3]
	v_cmp_ne_u64_e32 vcc, 0, v[8:9]
	s_and_b64 s[20:21], s[0:1], vcc
	s_cmp_lg_u64 s[20:21], 0
	s_cselect_b32 s20, 32768, 0
	s_or_b32 s76, s76, s20
	v_cmp_ne_u64_e32 vcc, -1, v[8:9]
	s_and_b64 s[20:21], s[0:1], vcc
	s_cmp_lg_u64 s[20:21], 0
	s_cselect_b32 s20, 32768, 0
	s_or_b32 s77, s77, s20
	v_lshl_add_u64 v[4:5], v[4:5], 0, 8
	v_mov_b32_e32 v2, s76
	v_mov_b32_e32 v8, s77
	s_mov_b64 s[2:3], exec
	s_mov_b64 exec, s[22:23]
	ds_write2_b32 v1, v2, v8 offset1:8
	s_mov_b64 exec, s[2:3]
	s_waitcnt lgkmcnt(0)
	s_barrier
	ds_read_b128 v[8:11], v3
	ds_read_b128 v[12:15], v3 offset:16
	ds_read_b128 v[16:19], v3 offset:32
	ds_read_b128 v[20:23], v3 offset:48
	s_waitcnt lgkmcnt(0)
	v_or_b32_e32 v8, v8, v9
	v_or3_b32 v8, v8, v10, v11
	v_or3_b32 v8, v8, v12, v13
	v_or3_b32 v8, v8, v14, v15
	v_or_b32_e32 v16, v16, v17
	v_or3_b32 v16, v16, v18, v19
	v_or3_b32 v16, v16, v20, v21
	v_or3_b32 v16, v16, v22, v23
	v_and_b32_e32 v2, 15, v0
	v_lshrrev_b32_e32 v8, v2, v8
	v_and_b32_e32 v8, 1, v8
	v_lshrrev_b32_e32 v16, v2, v16
	v_and_b32_e32 v16, 1, v16
	v_lshl_or_b32 v8, v16, 1, v8
	v_lshlrev_b32_e32 v2, 2, v2
	v_cmp_gt_u32_e32 vcc, 16, v0
	s_and_saveexec_b64 s[2:3], vcc
	global_store_dword v2, v8, s[26:27]
	s_mov_b64 exec, s[2:3]
